# NSA tile loop: lean common step (running DMA source pointer and slot offset in s32/s99-s101, counted wait without the ny dispatch)
# speedup vs baseline: 1.0085x; 1.0085x over previous
.LBB0_572:
	v_lshlrev_b32_e32 v202, 10, v3
	v_lshlrev_b32_e32 v203, 4, v198
	v_add3_u32 v69, 0, v202, v203
	ds_read_b128 v[4:7], v69
	ds_read_b128 v[8:11], v69 offset:512
	s_mov_b32 s0, 0xf149f2ca
	v_ashrrev_i32_e32 v182, 3, v68
	s_waitcnt lgkmcnt(1)
	v_mfma_f32_32x32x16_bf16 v[52:67], v[4:7], v[158:161], 0
	s_cmp_lt_i32 s82, 0
	s_waitcnt lgkmcnt(0)
	v_mfma_f32_32x32x16_bf16 v[36:51], v[8:11], v[158:161], 0
	ds_read_b128 v[4:7], v69 offset:2048
	ds_read_b128 v[8:11], v69 offset:2560
	s_waitcnt lgkmcnt(1)
	v_mfma_f32_32x32x16_bf16 v[52:67], v[4:7], v[154:157], v[52:67]
	s_waitcnt lgkmcnt(0)
	v_mfma_f32_32x32x16_bf16 v[36:51], v[8:11], v[154:157], v[36:51]
	ds_read_b128 v[4:7], v69 offset:4096
	ds_read_b128 v[8:11], v69 offset:4608
	s_waitcnt lgkmcnt(1)
	v_mfma_f32_32x32x16_bf16 v[52:67], v[4:7], v[150:153], v[52:67]
	s_waitcnt lgkmcnt(0)
	v_mfma_f32_32x32x16_bf16 v[36:51], v[8:11], v[150:153], v[36:51]
	ds_read_b128 v[4:7], v69 offset:6144
	ds_read_b128 v[8:11], v69 offset:6656
	s_waitcnt lgkmcnt(1)
	v_mfma_f32_32x32x16_bf16 v[52:67], v[4:7], v[146:149], v[52:67]
	s_waitcnt lgkmcnt(0)
	v_mfma_f32_32x32x16_bf16 v[36:51], v[8:11], v[146:149], v[36:51]
	ds_read_b128 v[4:7], v69 offset:16384
	ds_read_b128 v[8:11], v69 offset:16896
	ds_read_b128 v[74:77], v69 offset:18432
	ds_read_b128 v[78:81], v69 offset:18944
	s_waitcnt lgkmcnt(3)
	v_mfma_f32_32x32x16_bf16 v[20:35], v[4:7], v[158:161], 0
	s_waitcnt lgkmcnt(2)
	v_mfma_f32_32x32x16_bf16 v[4:19], v[8:11], v[158:161], 0
	s_waitcnt lgkmcnt(1)
	v_mfma_f32_32x32x16_bf16 v[20:35], v[74:77], v[154:157], v[20:35]
	s_waitcnt lgkmcnt(0)
	v_mfma_f32_32x32x16_bf16 v[4:19], v[78:81], v[154:157], v[4:19]
	ds_read_b128 v[74:77], v69 offset:20480
	ds_read_b128 v[78:81], v69 offset:20992
	s_waitcnt lgkmcnt(1)
	v_mfma_f32_32x32x16_bf16 v[20:35], v[74:77], v[150:153], v[20:35]
	s_waitcnt lgkmcnt(0)
	v_mfma_f32_32x32x16_bf16 v[4:19], v[78:81], v[150:153], v[4:19]
	ds_read_b128 v[74:77], v69 offset:22528
	ds_read_b128 v[78:81], v69 offset:23040
	v_lshlrev_b32_e32 v69, 6, v3
	v_sub_u32_e32 v69, v72, v69
	v_subrev_u32_e32 v72, 31, v69
	v_cmp_lt_i32_e32 vcc, -1, v72
	s_nop 1
	v_cndmask_b32_e32 v52, v195, v52, vcc
	v_cmp_lt_i32_e32 vcc, 15, v72
	s_waitcnt lgkmcnt(1)
	v_mfma_f32_32x32x16_bf16 v[20:35], v[74:77], v[146:149], v[20:35]
	v_cndmask_b32_e32 v53, v195, v53, vcc
	v_cmp_lt_i32_e32 vcc, 31, v72
	v_max3_f32 v69, v52, s0, v53
	s_movk_i32 s0, 0x7f
	v_cndmask_b32_e32 v54, v195, v54, vcc
	v_cmp_lt_i32_e32 vcc, 47, v72
	s_waitcnt lgkmcnt(0)
	v_mfma_f32_32x32x16_bf16 v[4:19], v[78:81], v[146:149], v[4:19]
	v_cndmask_b32_e32 v55, v195, v55, vcc
	v_cmp_lt_i32_e32 vcc, s0, v72
	s_movk_i32 s0, 0x8f
	v_max3_f32 v69, v69, v54, v55
	v_cndmask_b32_e32 v73, v195, v56, vcc
	v_cmp_lt_i32_e32 vcc, s0, v72
	s_movk_i32 s0, 0x9f
	s_nop 0
	v_cndmask_b32_e32 v74, v195, v57, vcc
	v_cmp_lt_i32_e32 vcc, s0, v72
	s_movk_i32 s0, 0xaf
	v_max3_f32 v56, v69, v73, v74
	v_cndmask_b32_e32 v75, v195, v58, vcc
	v_cmp_lt_i32_e32 vcc, s0, v72
	s_movk_i32 s0, 0xff
	s_nop 0
	v_cndmask_b32_e32 v76, v195, v59, vcc
	v_cmp_lt_i32_e32 vcc, s0, v72
	s_movk_i32 s0, 0x10f
	v_max3_f32 v56, v56, v75, v76
	v_cndmask_b32_e32 v77, v195, v60, vcc
	v_cmp_lt_i32_e32 vcc, s0, v72
	s_movk_i32 s0, 0x11f
	s_nop 0
	v_cndmask_b32_e32 v78, v195, v61, vcc
	v_cmp_lt_i32_e32 vcc, s0, v72
	s_movk_i32 s0, 0x12f
	v_max3_f32 v56, v56, v77, v78
	v_cndmask_b32_e32 v79, v195, v62, vcc
	v_cmp_lt_i32_e32 vcc, s0, v72
	s_movk_i32 s0, 0x17f
	s_nop 0
	v_cndmask_b32_e32 v80, v195, v63, vcc
	v_cmp_lt_i32_e32 vcc, s0, v72
	s_movk_i32 s0, 0x18f
	v_max3_f32 v56, v56, v79, v80
	v_cndmask_b32_e32 v81, v195, v64, vcc
	v_cmp_lt_i32_e32 vcc, s0, v72
	s_movk_i32 s0, 0x19f
	s_nop 0
	v_cndmask_b32_e32 v82, v195, v65, vcc
	v_cmp_lt_i32_e32 vcc, s0, v72
	s_movk_i32 s0, 0x1af
	v_max3_f32 v56, v56, v81, v82
	v_cndmask_b32_e32 v83, v195, v66, vcc
	v_cmp_lt_i32_e32 vcc, s0, v72
	s_movk_i32 s0, 0x1ff
	s_nop 0
	v_cndmask_b32_e32 v84, v195, v67, vcc
	v_cmp_lt_i32_e32 vcc, s0, v72
	s_movk_i32 s0, 0x20f
	v_max3_f32 v56, v56, v83, v84
	v_cndmask_b32_e32 v36, v195, v36, vcc
	v_cmp_lt_i32_e32 vcc, s0, v72
	s_movk_i32 s0, 0x21f
	s_nop 0
	v_cndmask_b32_e32 v37, v195, v37, vcc
	v_cmp_lt_i32_e32 vcc, s0, v72
	s_movk_i32 s0, 0x22f
	v_max3_f32 v56, v56, v36, v37
	v_cndmask_b32_e32 v38, v195, v38, vcc
	v_cmp_lt_i32_e32 vcc, s0, v72
	s_movk_i32 s0, 0x27f
	s_nop 0
	v_cndmask_b32_e32 v39, v195, v39, vcc
	v_cmp_lt_i32_e32 vcc, s0, v72
	s_movk_i32 s0, 0x28f
	v_max3_f32 v56, v56, v38, v39
	v_cndmask_b32_e32 v40, v195, v40, vcc
	v_cmp_lt_i32_e32 vcc, s0, v72
	s_movk_i32 s0, 0x29f
	s_nop 0
	v_cndmask_b32_e32 v41, v195, v41, vcc
	v_cmp_lt_i32_e32 vcc, s0, v72
	s_movk_i32 s0, 0x2af
	v_max3_f32 v56, v56, v40, v41
	v_cndmask_b32_e32 v42, v195, v42, vcc
	v_cmp_lt_i32_e32 vcc, s0, v72
	s_movk_i32 s0, 0x2ff
	s_nop 0
	v_cndmask_b32_e32 v43, v195, v43, vcc
	v_cmp_lt_i32_e32 vcc, s0, v72
	s_movk_i32 s0, 0x30f
	v_max3_f32 v56, v56, v42, v43
	v_cndmask_b32_e32 v44, v195, v44, vcc
	v_cmp_lt_i32_e32 vcc, s0, v72
	s_movk_i32 s0, 0x31f
	s_nop 0
	v_cndmask_b32_e32 v45, v195, v45, vcc
	v_cmp_lt_i32_e32 vcc, s0, v72
	s_movk_i32 s0, 0x32f
	v_max3_f32 v56, v56, v44, v45
	v_cndmask_b32_e32 v46, v195, v46, vcc
	v_cmp_lt_i32_e32 vcc, s0, v72
	s_movk_i32 s0, 0x37f
	s_nop 0
	v_cndmask_b32_e32 v47, v195, v47, vcc
	v_cmp_lt_i32_e32 vcc, s0, v72
	s_movk_i32 s0, 0x38f
	v_max3_f32 v56, v56, v46, v47
	v_cndmask_b32_e32 v48, v195, v48, vcc
	v_cmp_lt_i32_e32 vcc, s0, v72
	s_movk_i32 s0, 0x39f
	s_nop 0
	v_cndmask_b32_e32 v49, v195, v49, vcc
	v_cmp_lt_i32_e32 vcc, s0, v72
	s_movk_i32 s0, 0x3af
	v_max3_f32 v56, v56, v48, v49
	v_cndmask_b32_e32 v50, v195, v50, vcc
	v_cmp_lt_i32_e32 vcc, s0, v72
	s_movk_i32 s0, 0x40f
	s_nop 0
	v_cndmask_b32_e32 v51, v195, v51, vcc
	v_cmp_lt_i32_e32 vcc, s39, v72
	v_max3_f32 v56, v56, v50, v51
	s_nop 0
	v_cndmask_b32_e32 v85, v195, v20, vcc
	v_cmp_lt_i32_e32 vcc, s0, v72
	s_movk_i32 s0, 0x41f
	s_nop 0
	v_cndmask_b32_e32 v86, v195, v21, vcc
	v_cmp_lt_i32_e32 vcc, s0, v72
	s_movk_i32 s0, 0x42f
	v_max3_f32 v20, v56, v85, v86
	v_cndmask_b32_e32 v87, v195, v22, vcc
	v_cmp_lt_i32_e32 vcc, s0, v72
	s_movk_i32 s0, 0x47f
	s_nop 0
	v_cndmask_b32_e32 v88, v195, v23, vcc
	v_cmp_lt_i32_e32 vcc, s0, v72
	s_movk_i32 s0, 0x48f
	v_max3_f32 v20, v20, v87, v88
	v_cndmask_b32_e32 v89, v195, v24, vcc
	v_cmp_lt_i32_e32 vcc, s0, v72
	s_movk_i32 s0, 0x49f
	s_nop 0
	v_cndmask_b32_e32 v90, v195, v25, vcc
	v_cmp_lt_i32_e32 vcc, s0, v72
	s_movk_i32 s0, 0x4af
	v_max3_f32 v20, v20, v89, v90
	v_cndmask_b32_e32 v91, v195, v26, vcc
	v_cmp_lt_i32_e32 vcc, s0, v72
	s_movk_i32 s0, 0x4ff
	s_nop 0
	v_cndmask_b32_e32 v92, v195, v27, vcc
	v_cmp_lt_i32_e32 vcc, s0, v72
	s_movk_i32 s0, 0x50f
	v_max3_f32 v20, v20, v91, v92
	v_cndmask_b32_e32 v93, v195, v28, vcc
	v_cmp_lt_i32_e32 vcc, s0, v72
	s_movk_i32 s0, 0x51f
	s_nop 0
	v_cndmask_b32_e32 v94, v195, v29, vcc
	v_cmp_lt_i32_e32 vcc, s0, v72
	s_movk_i32 s0, 0x52f
	v_max3_f32 v20, v20, v93, v94
	v_cndmask_b32_e32 v95, v195, v30, vcc
	v_cmp_lt_i32_e32 vcc, s0, v72
	s_movk_i32 s0, 0x57f
	s_nop 0
	v_cndmask_b32_e32 v96, v195, v31, vcc
	v_cmp_lt_i32_e32 vcc, s0, v72
	s_movk_i32 s0, 0x58f
	v_max3_f32 v20, v20, v95, v96
	v_cndmask_b32_e32 v97, v195, v32, vcc
	v_cmp_lt_i32_e32 vcc, s0, v72
	s_movk_i32 s0, 0x59f
	s_nop 0
	v_cndmask_b32_e32 v98, v195, v33, vcc
	v_cmp_lt_i32_e32 vcc, s0, v72
	s_movk_i32 s0, 0x5af
	v_max3_f32 v20, v20, v97, v98
	v_cndmask_b32_e32 v99, v195, v34, vcc
	v_cmp_lt_i32_e32 vcc, s0, v72
	s_movk_i32 s0, 0x5ff
	s_nop 0
	v_cndmask_b32_e32 v100, v195, v35, vcc
	v_cmp_lt_i32_e32 vcc, s0, v72
	s_movk_i32 s0, 0x60f
	v_max3_f32 v20, v20, v99, v100
	v_cndmask_b32_e32 v101, v195, v4, vcc
	v_cmp_lt_i32_e32 vcc, s0, v72
	s_movk_i32 s0, 0x61f
	s_nop 0
	v_cndmask_b32_e32 v102, v195, v5, vcc
	v_cmp_lt_i32_e32 vcc, s0, v72
	s_movk_i32 s0, 0x62f
	v_max3_f32 v4, v20, v101, v102
	v_cndmask_b32_e32 v103, v195, v6, vcc
	v_cmp_lt_i32_e32 vcc, s0, v72
	s_movk_i32 s0, 0x67f
	s_nop 0
	v_cndmask_b32_e32 v104, v195, v7, vcc
	v_cmp_lt_i32_e32 vcc, s0, v72
	s_movk_i32 s0, 0x68f
	v_max3_f32 v4, v4, v103, v104
	v_cndmask_b32_e32 v58, v195, v8, vcc
	v_cmp_lt_i32_e32 vcc, s0, v72
	s_movk_i32 s0, 0x69f
	s_nop 0
	v_cndmask_b32_e32 v59, v195, v9, vcc
	v_cmp_lt_i32_e32 vcc, s0, v72
	s_movk_i32 s0, 0x6af
	v_max3_f32 v4, v4, v58, v59
	v_cndmask_b32_e32 v56, v195, v10, vcc
	v_cmp_lt_i32_e32 vcc, s0, v72
	s_movk_i32 s0, 0x6ff
	s_nop 0
	v_cndmask_b32_e32 v57, v195, v11, vcc
	v_cmp_lt_i32_e32 vcc, s0, v72
	s_movk_i32 s0, 0x70f
	v_max3_f32 v4, v4, v56, v57
	v_cndmask_b32_e32 v62, v195, v12, vcc
	v_cmp_lt_i32_e32 vcc, s0, v72
	s_movk_i32 s0, 0x71f
	s_nop 0
	v_cndmask_b32_e32 v63, v195, v13, vcc
	v_cmp_lt_i32_e32 vcc, s0, v72
	s_movk_i32 s0, 0x72f
	v_max3_f32 v4, v4, v62, v63
	v_cndmask_b32_e32 v60, v195, v14, vcc
	v_cmp_lt_i32_e32 vcc, s0, v72
	s_movk_i32 s0, 0x77f
	s_nop 0
	v_cndmask_b32_e32 v61, v195, v15, vcc
	v_cmp_lt_i32_e32 vcc, s0, v72
	s_movk_i32 s0, 0x78f
	v_max3_f32 v4, v4, v60, v61
	v_cndmask_b32_e32 v69, v195, v16, vcc
	v_cmp_lt_i32_e32 vcc, s0, v72
	s_movk_i32 s0, 0x79f
	s_nop 0
	v_cndmask_b32_e32 v66, v195, v17, vcc
	v_cmp_lt_i32_e32 vcc, s0, v72
	s_movk_i32 s0, 0x7af
	v_max3_f32 v4, v4, v69, v66
	v_cndmask_b32_e32 v65, v195, v18, vcc
	v_cmp_lt_i32_e32 vcc, s0, v72
	s_mov_b32 s0, 0xefa18f08
	s_nop 0
	v_cndmask_b32_e32 v64, v195, v19, vcc
	v_max3_f32 v4, v4, v65, v64
	v_mov_b32_e32 v5, v4
	s_nop 1
	v_permlane32_swap_b32_e32 v4, v5
	v_max3_f32 v67, v4, v5, s0
	v_sub_f32_e32 v4, v52, v67
	v_exp_f32_e32 v4, v4
	v_sub_f32_e32 v5, v53, v67
	v_exp_f32_e32 v5, v5
	v_sub_f32_e32 v9, v73, v67
	v_add_f32_e32 v6, 0, v4
	v_exp_f32_e32 v10, v9
	v_add_f32_e32 v7, v5, v6
	v_sub_f32_e32 v6, v54, v67
	v_exp_f32_e32 v6, v6
	v_sub_f32_e32 v9, v74, v67
	v_exp_f32_e32 v11, v9
	v_sub_f32_e32 v13, v77, v67
	v_add_f32_e32 v8, v6, v7
	v_sub_f32_e32 v7, v55, v67
	v_exp_f32_e32 v7, v7
	v_exp_f32_e32 v14, v13
	v_sub_f32_e32 v13, v78, v67
	v_exp_f32_e32 v15, v13
	v_add_f32_e32 v8, v7, v8
	v_add_f32_e32 v8, v10, v8
	v_add_f32_e32 v9, v11, v8
	v_sub_f32_e32 v8, v75, v67
	v_exp_f32_e32 v8, v8
	v_sub_f32_e32 v17, v81, v67
	v_exp_f32_e32 v18, v17
	v_sub_f32_e32 v17, v82, v67
	v_add_f32_e32 v12, v8, v9
	v_sub_f32_e32 v9, v76, v67
	v_exp_f32_e32 v9, v9
	v_exp_f32_e32 v19, v17
	v_sub_f32_e32 v21, v36, v67
	v_exp_f32_e32 v22, v21
	v_add_f32_e32 v12, v9, v12
	v_add_f32_e32 v12, v14, v12
	v_add_f32_e32 v13, v15, v12
	v_sub_f32_e32 v12, v79, v67
	v_exp_f32_e32 v12, v12
	v_sub_f32_e32 v21, v37, v67
	v_exp_f32_e32 v23, v21
	v_sub_f32_e32 v25, v40, v67
	v_add_f32_e32 v16, v12, v13
	v_sub_f32_e32 v13, v80, v67
	v_exp_f32_e32 v13, v13
	v_exp_f32_e32 v26, v25
	v_sub_f32_e32 v25, v41, v67
	v_exp_f32_e32 v27, v25
	v_add_f32_e32 v16, v13, v16
	v_add_f32_e32 v16, v18, v16
	v_add_f32_e32 v17, v19, v16
	v_sub_f32_e32 v16, v83, v67
	v_exp_f32_e32 v16, v16
	v_sub_f32_e32 v29, v44, v67
	v_exp_f32_e32 v30, v29
	v_sub_f32_e32 v29, v45, v67
	v_add_f32_e32 v20, v16, v17
	v_sub_f32_e32 v17, v84, v67
	v_exp_f32_e32 v17, v17
	v_exp_f32_e32 v31, v29
	v_sub_f32_e32 v33, v48, v67
	v_exp_f32_e32 v34, v33
	v_add_f32_e32 v20, v17, v20
	v_add_f32_e32 v20, v22, v20
	v_add_f32_e32 v21, v23, v20
	v_sub_f32_e32 v20, v38, v67
	v_exp_f32_e32 v20, v20
	v_sub_f32_e32 v33, v49, v67
	v_exp_f32_e32 v35, v33
	v_sub_f32_e32 v37, v85, v67
	v_add_f32_e32 v24, v20, v21
	v_sub_f32_e32 v21, v39, v67
	v_exp_f32_e32 v21, v21
	v_exp_f32_e32 v38, v37
	v_sub_f32_e32 v37, v86, v67
	v_exp_f32_e32 v39, v37
	v_add_f32_e32 v24, v21, v24
	v_add_f32_e32 v24, v26, v24
	v_add_f32_e32 v25, v27, v24
	v_sub_f32_e32 v24, v42, v67
	v_exp_f32_e32 v24, v24
	v_sub_f32_e32 v41, v89, v67
	v_exp_f32_e32 v42, v41
	v_sub_f32_e32 v41, v90, v67
	v_add_f32_e32 v28, v24, v25
	v_sub_f32_e32 v25, v43, v67
	v_exp_f32_e32 v25, v25
	v_exp_f32_e32 v43, v41
	v_sub_f32_e32 v45, v93, v67
	v_sub_f32_e32 v49, v97, v67
	v_add_f32_e32 v28, v25, v28
	v_add_f32_e32 v28, v30, v28
	v_add_f32_e32 v29, v31, v28
	v_sub_f32_e32 v28, v46, v67
	v_exp_f32_e32 v28, v28
	v_exp_f32_e32 v46, v45
	v_sub_f32_e32 v45, v94, v67
	v_sub_f32_e32 v53, v101, v67
	v_add_f32_e32 v32, v28, v29
	v_sub_f32_e32 v29, v47, v67
	v_exp_f32_e32 v29, v29
	v_exp_f32_e32 v47, v45
	v_exp_f32_e32 v54, v53
	v_sub_f32_e32 v53, v102, v67
	v_add_f32_e32 v32, v29, v32
	v_add_f32_e32 v32, v34, v32
	v_add_f32_e32 v33, v35, v32
	v_sub_f32_e32 v32, v50, v67
	v_exp_f32_e32 v32, v32
	v_exp_f32_e32 v50, v49
	v_sub_f32_e32 v49, v98, v67
	v_exp_f32_e32 v55, v53
	v_add_f32_e32 v36, v32, v33
	v_sub_f32_e32 v33, v51, v67
	v_exp_f32_e32 v33, v33
	v_exp_f32_e32 v51, v49
	v_sub_f32_e32 v58, v58, v67
	v_exp_f32_e32 v58, v58
	v_add_f32_e32 v36, v33, v36
	v_add_f32_e32 v36, v38, v36
	v_add_f32_e32 v37, v39, v36
	v_sub_f32_e32 v36, v87, v67
	v_exp_f32_e32 v36, v36
	v_sub_f32_e32 v59, v59, v67
	v_exp_f32_e32 v59, v59
	v_sub_f32_e32 v56, v56, v67
	v_add_f32_e32 v40, v36, v37
	v_sub_f32_e32 v37, v88, v67
	v_exp_f32_e32 v37, v37
	v_exp_f32_e32 v56, v56
	v_sub_f32_e32 v57, v57, v67
	v_exp_f32_e32 v57, v57
	v_add_f32_e32 v40, v37, v40
	v_add_f32_e32 v40, v42, v40
	v_add_f32_e32 v41, v43, v40
	v_sub_f32_e32 v40, v91, v67
	v_exp_f32_e32 v40, v40
	v_sub_f32_e32 v62, v62, v67
	v_exp_f32_e32 v62, v62
	v_sub_f32_e32 v63, v63, v67
	v_add_f32_e32 v44, v40, v41
	v_sub_f32_e32 v41, v92, v67
	v_exp_f32_e32 v41, v41
	v_exp_f32_e32 v63, v63
	v_sub_f32_e32 v60, v60, v67
	v_exp_f32_e32 v60, v60
	v_add_f32_e32 v44, v41, v44
	v_add_f32_e32 v44, v46, v44
	v_add_f32_e32 v45, v47, v44
	v_sub_f32_e32 v44, v95, v67
	v_exp_f32_e32 v44, v44
	v_sub_f32_e32 v61, v61, v67
	v_exp_f32_e32 v61, v61
	v_sub_f32_e32 v69, v69, v67
	v_add_f32_e32 v48, v44, v45
	v_sub_f32_e32 v45, v96, v67
	v_exp_f32_e32 v45, v45
	v_sub_f32_e32 v66, v66, v67
	v_sub_f32_e32 v65, v65, v67
	v_sub_f32_e32 v64, v64, v67
	v_add_f32_e32 v48, v45, v48
	v_add_f32_e32 v48, v50, v48
	v_add_f32_e32 v49, v51, v48
	v_sub_f32_e32 v48, v99, v67
	v_exp_f32_e32 v48, v48
	s_nop 0
	v_add_f32_e32 v52, v48, v49
	v_sub_f32_e32 v49, v100, v67
	v_exp_f32_e32 v49, v49
	s_nop 0
	v_add_f32_e32 v52, v49, v52
	v_add_f32_e32 v52, v54, v52
	v_add_f32_e32 v53, v55, v52
	v_sub_f32_e32 v52, v103, v67
	v_exp_f32_e32 v52, v52
	s_nop 0
	v_add_f32_e32 v72, v52, v53
	v_sub_f32_e32 v53, v104, v67
	v_exp_f32_e32 v53, v53
	v_exp_f32_e32 v67, v64
	v_add_f32_e32 v72, v53, v72
	v_add_f32_e32 v72, v58, v72
	v_add_f32_e32 v72, v59, v72
	v_add_f32_e32 v72, v56, v72
	v_add_f32_e32 v72, v57, v72
	v_add_f32_e32 v72, v62, v72
	v_add_f32_e32 v72, v63, v72
	v_add_f32_e32 v72, v60, v72
	v_add_f32_e32 v73, v61, v72
	v_exp_f32_e32 v72, v69
	s_nop 0
	v_add_f32_e32 v69, v72, v73
	v_exp_f32_e32 v73, v66
	v_exp_f32_e32 v66, v65
	v_add_f32_e32 v69, v73, v69
	v_add_f32_e32 v65, v66, v69
	v_add_f32_e32 v64, v67, v65
	v_mov_b32_e32 v65, v64
	s_nop 1
	v_permlane32_swap_b32_e32 v64, v65
	v_add_f32_e32 v64, v64, v65
	v_div_scale_f32 v65, s[2:3], v64, v64, 1.0
	v_rcp_f32_e32 v69, v65
	v_cmp_lt_f32_e64 s[0:1], 0, v64
	v_fma_f32 v74, -v65, v69, 1.0
	v_fmac_f32_e32 v69, v74, v69
	v_div_scale_f32 v74, vcc, 1.0, v64, 1.0
	v_mul_f32_e32 v75, v74, v69
	v_fma_f32 v76, -v65, v75, v74
	v_fmac_f32_e32 v75, v76, v69
	v_fma_f32 v65, -v65, v75, v74
	v_div_fmas_f32 v65, v65, v69, v75
	v_and_b32_e32 v69, 64, v212
	v_div_fixup_f32 v64, v65, v64, 1.0
	v_xor_b32_e32 v65, 32, v212
	v_add_u32_e32 v69, 64, v69
	v_cmp_lt_i32_e32 vcc, v65, v69
	v_cndmask_b32_e64 v76, 0, v64, s[0:1]
	v_add_u32_e32 v64, s12, v71
	v_cndmask_b32_e32 v65, v212, v65, vcc
	v_lshlrev_b32_e32 v77, 2, v65
	v_pk_mul_f32 v[6:7], v[6:7], v[76:77] op_sel_hi:[1,0]
	ds_bpermute_b32 v74, v77, v7
	v_mul_lo_u32 v64, v64, s64
	v_lshlrev_b32_e32 v69, 2, v3
	v_add3_u32 v88, s33, v64, v69
	v_pk_mul_f32 v[64:65], v[4:5], v[76:77] op_sel_hi:[1,0]
	v_cmp_gt_u32_e32 vcc, 32, v68
	v_pk_mul_f32 v[4:5], v[70:71], v[64:65] op_sel_hi:[0,1]
	v_add_f32_e32 v75, v6, v7
	v_add_f32_e32 v64, v64, v65
	v_add_f32_e32 v64, v64, v75
	s_waitcnt lgkmcnt(0)
	v_cndmask_b32_e64 v65, v74, 0, vcc
	v_pk_mul_f32 v[8:9], v[8:9], v[76:77] op_sel_hi:[1,0]
	v_add_f32_e32 v64, v65, v64
	ds_bpermute_b32 v65, v77, v9
	v_pk_mul_f32 v[10:11], v[10:11], v[76:77] op_sel_hi:[1,0]
	v_add_f32_e32 v75, v8, v9
	v_pk_mul_f32 v[78:79], v[70:71], v[10:11] op_sel_hi:[0,1]
	v_add_f32_e32 v10, v10, v11
	v_add_f32_e32 v10, v10, v75
	s_waitcnt lgkmcnt(0)
	v_cndmask_b32_e32 v11, v65, v74, vcc
	v_add_f32_e32 v10, v11, v10
	ds_write2_b32 v88, v64, v10 offset1:2
	v_pk_mul_f32 v[10:11], v[12:13], v[76:77] op_sel_hi:[1,0]
	ds_bpermute_b32 v12, v77, v11
	v_add_f32_e32 v13, v10, v11
	v_pk_mul_f32 v[84:85], v[70:71], v[10:11] op_sel_hi:[0,1]
	v_pk_mul_f32 v[10:11], v[16:17], v[76:77] op_sel_hi:[1,0]
	v_pk_mul_f32 v[80:81], v[70:71], v[8:9] op_sel_hi:[0,1]
	v_pk_mul_f32 v[8:9], v[14:15], v[76:77] op_sel_hi:[1,0]
	ds_bpermute_b32 v14, v77, v11
	v_pk_mul_f32 v[82:83], v[70:71], v[8:9] op_sel_hi:[0,1]
	v_add_f32_e32 v8, v8, v9
	v_add_f32_e32 v8, v8, v13
	s_waitcnt lgkmcnt(1)
	v_cndmask_b32_e32 v9, v12, v65, vcc
	v_add_f32_e32 v13, v9, v8
	v_pk_mul_f32 v[8:9], v[18:19], v[76:77] op_sel_hi:[1,0]
	v_add_f32_e32 v15, v10, v11
	v_pk_mul_f32 v[86:87], v[70:71], v[10:11] op_sel_hi:[0,1]
	v_pk_mul_f32 v[10:11], v[20:21], v[76:77] op_sel_hi:[1,0]
	v_pk_mul_f32 v[18:19], v[70:71], v[8:9] op_sel_hi:[0,1]
	v_add_f32_e32 v8, v8, v9
	s_waitcnt lgkmcnt(0)
	v_cndmask_b32_e32 v9, v14, v12, vcc
	ds_bpermute_b32 v12, v77, v11
	v_add_f32_e32 v8, v8, v15
	v_add_f32_e32 v8, v9, v8
	ds_write2_b32 v88, v13, v8 offset0:4 offset1:6
	v_pk_mul_f32 v[8:9], v[22:23], v[76:77] op_sel_hi:[1,0]
	v_add_f32_e32 v13, v10, v11
	v_pk_mul_f32 v[20:21], v[70:71], v[10:11] op_sel_hi:[0,1]
	v_pk_mul_f32 v[10:11], v[24:25], v[76:77] op_sel_hi:[1,0]
	v_pk_mul_f32 v[22:23], v[70:71], v[8:9] op_sel_hi:[0,1]
	v_add_f32_e32 v8, v8, v9
	s_waitcnt lgkmcnt(1)
	v_cndmask_b32_e32 v9, v12, v14, vcc
	ds_bpermute_b32 v14, v77, v11
	v_add_f32_e32 v8, v8, v13
	v_add_f32_e32 v13, v8, v9
	v_pk_mul_f32 v[8:9], v[26:27], v[76:77] op_sel_hi:[1,0]
	v_add_f32_e32 v15, v10, v11
	v_pk_mul_f32 v[24:25], v[70:71], v[10:11] op_sel_hi:[0,1]
	v_pk_mul_f32 v[10:11], v[28:29], v[76:77] op_sel_hi:[1,0]
	v_pk_mul_f32 v[26:27], v[70:71], v[8:9] op_sel_hi:[0,1]
	v_add_f32_e32 v8, v8, v9
	s_waitcnt lgkmcnt(0)
	v_cndmask_b32_e32 v9, v14, v12, vcc
	ds_bpermute_b32 v12, v77, v11
	v_add_f32_e32 v8, v8, v15
	v_add_f32_e32 v8, v8, v9
	ds_write2_b32 v88, v13, v8 offset0:8 offset1:10
	v_pk_mul_f32 v[8:9], v[30:31], v[76:77] op_sel_hi:[1,0]
	v_add_f32_e32 v13, v10, v11
	v_pk_mul_f32 v[28:29], v[70:71], v[10:11] op_sel_hi:[0,1]
	v_pk_mul_f32 v[10:11], v[32:33], v[76:77] op_sel_hi:[1,0]
	v_pk_mul_f32 v[30:31], v[70:71], v[8:9] op_sel_hi:[0,1]
	v_add_f32_e32 v8, v8, v9
	s_waitcnt lgkmcnt(1)
	v_cndmask_b32_e32 v9, v12, v14, vcc
	ds_bpermute_b32 v14, v77, v11
	v_add_f32_e32 v8, v8, v13
	v_add_f32_e32 v13, v8, v9
	v_pk_mul_f32 v[8:9], v[34:35], v[76:77] op_sel_hi:[1,0]
	v_add_f32_e32 v15, v10, v11
	v_pk_mul_f32 v[34:35], v[70:71], v[8:9] op_sel_hi:[0,1]
	v_add_f32_e32 v8, v8, v9
	v_add_f32_e32 v8, v8, v15
	s_waitcnt lgkmcnt(0)
	v_cndmask_b32_e32 v9, v14, v12, vcc
	v_add_f32_e32 v8, v8, v9
	ds_write2_b32 v88, v13, v8 offset0:12 offset1:14
	v_pk_mul_f32 v[12:13], v[36:37], v[76:77] op_sel_hi:[1,0]
	ds_bpermute_b32 v36, v77, v13
	v_pk_mul_f32 v[16:17], v[40:41], v[76:77] op_sel_hi:[1,0]
	ds_bpermute_b32 v40, v77, v17
	v_pk_mul_f32 v[32:33], v[70:71], v[10:11] op_sel_hi:[0,1]
	v_pk_mul_f32 v[10:11], v[38:39], v[76:77] op_sel_hi:[1,0]
	v_add_f32_e32 v15, v12, v13
	v_pk_mul_f32 v[8:9], v[70:71], v[10:11] op_sel_hi:[0,1]
	v_add_f32_e32 v10, v10, v11
	v_add_f32_e32 v10, v10, v15
	s_waitcnt lgkmcnt(1)
	v_cndmask_b32_e32 v11, v36, v14, vcc
	v_pk_mul_f32 v[14:15], v[42:43], v[76:77] op_sel_hi:[1,0]
	v_add_f32_e32 v37, v10, v11
	v_pk_mul_f32 v[10:11], v[70:71], v[12:13] op_sel_hi:[0,1]
	v_pk_mul_f32 v[12:13], v[70:71], v[14:15] op_sel_hi:[0,1]
	v_add_f32_e32 v38, v16, v17
	v_add_f32_e32 v14, v14, v15
	v_add_f32_e32 v14, v14, v38
	s_waitcnt lgkmcnt(0)
	v_cndmask_b32_e32 v15, v40, v36, vcc
	v_pk_mul_f32 v[38:39], v[44:45], v[76:77] op_sel_hi:[1,0]
	v_add_f32_e32 v14, v14, v15
	ds_bpermute_b32 v41, v77, v39
	ds_write2_b32 v88, v37, v14 offset0:16 offset1:18
	v_pk_mul_f32 v[36:37], v[46:47], v[76:77] op_sel_hi:[1,0]
	v_pk_mul_f32 v[14:15], v[70:71], v[16:17] op_sel_hi:[0,1]
	v_pk_mul_f32 v[16:17], v[70:71], v[36:37] op_sel_hi:[0,1]
	v_add_f32_e32 v42, v38, v39
	v_add_f32_e32 v36, v36, v37
	v_pk_mul_f32 v[64:65], v[70:71], v[38:39] op_sel_hi:[0,1]
	v_pk_mul_f32 v[38:39], v[48:49], v[76:77] op_sel_hi:[1,0]
	v_add_f32_e32 v36, v36, v42
	ds_bpermute_b32 v42, v77, v39
	s_waitcnt lgkmcnt(2)
	v_cndmask_b32_e32 v37, v41, v40, vcc
	v_add_f32_e32 v40, v36, v37
	v_pk_mul_f32 v[36:37], v[50:51], v[76:77] op_sel_hi:[1,0]
	v_add_f32_e32 v43, v38, v39
	v_pk_mul_f32 v[50:51], v[70:71], v[36:37] op_sel_hi:[0,1]
	v_add_f32_e32 v36, v36, v37
	v_add_f32_e32 v36, v36, v43
	s_waitcnt lgkmcnt(0)
	v_cndmask_b32_e32 v37, v42, v41, vcc
	v_add_f32_e32 v36, v36, v37
	v_pk_mul_f32 v[74:75], v[70:71], v[38:39] op_sel_hi:[0,1]
	v_pk_mul_f32 v[38:39], v[52:53], v[76:77] op_sel_hi:[1,0]
	ds_write2_b32 v88, v40, v36 offset0:20 offset1:22
	ds_bpermute_b32 v40, v77, v39
	v_pk_mul_f32 v[36:37], v[54:55], v[76:77] op_sel_hi:[1,0]
	v_add_f32_e32 v41, v38, v39
	v_pk_mul_f32 v[52:53], v[70:71], v[38:39] op_sel_hi:[0,1]
	v_pk_mul_f32 v[38:39], v[56:57], v[76:77] op_sel_hi:[1,0]
	v_pk_mul_f32 v[54:55], v[70:71], v[36:37] op_sel_hi:[0,1]
	v_add_f32_e32 v36, v36, v37
	s_waitcnt lgkmcnt(0)
	v_cndmask_b32_e32 v37, v40, v42, vcc
	ds_bpermute_b32 v42, v77, v39
	v_add_f32_e32 v36, v36, v41
	v_add_f32_e32 v41, v36, v37
	v_pk_mul_f32 v[36:37], v[58:59], v[76:77] op_sel_hi:[1,0]
	v_add_f32_e32 v43, v38, v39
	v_pk_mul_f32 v[56:57], v[70:71], v[38:39] op_sel_hi:[0,1]
	v_pk_mul_f32 v[38:39], v[60:61], v[76:77] op_sel_hi:[1,0]
	v_pk_mul_f32 v[58:59], v[70:71], v[36:37] op_sel_hi:[0,1]
	v_add_f32_e32 v36, v36, v37
	s_waitcnt lgkmcnt(0)
	v_cndmask_b32_e32 v37, v42, v40, vcc
	ds_bpermute_b32 v40, v77, v39
	v_add_f32_e32 v36, v36, v43
	v_add_f32_e32 v36, v36, v37
	ds_write2_b32 v88, v41, v36 offset0:24 offset1:26
	v_pk_mul_f32 v[36:37], v[62:63], v[76:77] op_sel_hi:[1,0]
	v_add_f32_e32 v41, v38, v39
	v_pk_mul_f32 v[60:61], v[70:71], v[38:39] op_sel_hi:[0,1]
	v_pk_mul_f32 v[38:39], v[66:67], v[76:77] op_sel_hi:[1,0]
	v_pk_mul_f32 v[62:63], v[70:71], v[36:37] op_sel_hi:[0,1]
	v_add_f32_e32 v36, v36, v37
	s_waitcnt lgkmcnt(1)
	v_cndmask_b32_e32 v37, v40, v42, vcc
	ds_bpermute_b32 v42, v77, v39
	v_add_f32_e32 v36, v36, v41
	v_add_f32_e32 v41, v36, v37
	v_pk_mul_f32 v[36:37], v[72:73], v[76:77] op_sel_hi:[1,0]
	v_add_f32_e32 v43, v38, v39
	v_pk_mul_f32 v[72:73], v[70:71], v[36:37] op_sel_hi:[0,1]
	v_add_f32_e32 v36, v36, v37
	v_cvt_pk_bf16_f32 v78, v78, v79
	v_cvt_pk_bf16_f32 v79, v80, v81
	v_cvt_pk_bf16_f32 v80, v82, v83
	v_cvt_pk_bf16_f32 v82, v18, v19
	v_lshlrev_b32_e32 v18, 1, v68
	v_bfe_u32 v19, v68, 2, 2
	s_mov_b32 s0, 0x3fffffc
	v_add_f32_e32 v36, v36, v43
	s_waitcnt lgkmcnt(0)
	v_cndmask_b32_e32 v37, v42, v40, vcc
	v_and_b32_e32 v204, 32, v18
	v_and_or_b32 v19, v182, s0, v19
	v_add_f32_e32 v36, v36, v37
	v_add_u32_e32 v18, 0, v204
	v_lshlrev_b32_e32 v205, 6, v19
	v_pk_mul_f32 v[6:7], v[70:71], v[6:7] op_sel_hi:[0,1]
	ds_write2_b32 v88, v41, v36 offset0:28 offset1:30
	v_pk_mul_f32 v[66:67], v[70:71], v[38:39] op_sel_hi:[0,1]
	v_add3_u32 v70, v18, v201, v205
	v_cvt_pk_bf16_f32 v81, v84, v85
	v_cvt_pk_bf16_f32 v83, v86, v87
	v_cvt_pk_bf16_f32 v84, v22, v23
	v_cvt_pk_bf16_f32 v85, v20, v21
	v_cvt_pk_bf16_f32 v87, v24, v25
	ds_read_b64_tr_b16 v[18:19], v70 offset:8192
	ds_read_b64_tr_b16 v[20:21], v70 offset:8704
	ds_read_b64_tr_b16 v[22:23], v70 offset:12288
	ds_read_b64_tr_b16 v[24:25], v70 offset:12800
	v_cvt_pk_bf16_f32 v76, v4, v5
	v_cvt_pk_bf16_f32 v77, v6, v7
	v_cvt_pk_bf16_f32 v86, v26, v27
	v_cvt_pk_bf16_f32 v4, v30, v31
	v_cvt_pk_bf16_f32 v5, v28, v29
	v_cvt_pk_bf16_f32 v6, v34, v35
	v_cvt_pk_bf16_f32 v7, v32, v33
	s_waitcnt lgkmcnt(2)
	v_mfma_f32_32x32x16_bf16 v[34:49], v[18:21], v[76:79], 0
	s_waitcnt lgkmcnt(0)
	v_mfma_f32_32x32x16_bf16 v[18:33], v[22:25], v[76:79], 0
	ds_read_b64_tr_b16 v[76:77], v70 offset:9216
	ds_read_b64_tr_b16 v[78:79], v70 offset:9728
	ds_read_b64_tr_b16 v[88:89], v70 offset:13312
	ds_read_b64_tr_b16 v[90:91], v70 offset:13824
	s_waitcnt lgkmcnt(2)
	v_mfma_f32_32x32x16_bf16 v[34:49], v[76:79], v[80:83], v[34:49]
	s_waitcnt lgkmcnt(0)
	v_mfma_f32_32x32x16_bf16 v[18:33], v[88:91], v[80:83], v[18:33]
	ds_read_b64_tr_b16 v[76:77], v70 offset:10240
	ds_read_b64_tr_b16 v[78:79], v70 offset:10752
	ds_read_b64_tr_b16 v[80:81], v70 offset:14336
	ds_read_b64_tr_b16 v[82:83], v70 offset:14848
	s_waitcnt lgkmcnt(2)
	v_mfma_f32_32x32x16_bf16 v[34:49], v[76:79], v[84:87], v[34:49]
	s_waitcnt lgkmcnt(0)
	v_mfma_f32_32x32x16_bf16 v[18:33], v[80:83], v[84:87], v[18:33]
	ds_read_b64_tr_b16 v[76:77], v70 offset:11264
	ds_read_b64_tr_b16 v[78:79], v70 offset:11776
	ds_read_b64_tr_b16 v[80:81], v70 offset:15360
	ds_read_b64_tr_b16 v[82:83], v70 offset:15872
	s_waitcnt lgkmcnt(2)
	v_mfma_f32_32x32x16_bf16 v[34:49], v[76:79], v[4:7], v[34:49]
	v_cvt_pk_bf16_f32 v76, v8, v9
	v_cvt_pk_bf16_f32 v77, v10, v11
	v_cvt_pk_bf16_f32 v79, v14, v15
	v_cvt_pk_bf16_f32 v14, v50, v51
	v_cvt_pk_bf16_f32 v8, v54, v55
	v_cvt_pk_bf16_f32 v9, v52, v53
	v_cvt_pk_bf16_f32 v11, v56, v57
	s_waitcnt lgkmcnt(0)
	v_mfma_f32_32x32x16_bf16 v[18:33], v[80:83], v[4:7], v[18:33]
	ds_read_b64_tr_b16 v[50:51], v70 offset:24576
	ds_read_b64_tr_b16 v[52:53], v70 offset:25088
	ds_read_b64_tr_b16 v[54:55], v70 offset:28672
	ds_read_b64_tr_b16 v[56:57], v70 offset:29184
	v_cvt_pk_bf16_f32 v78, v12, v13
	v_cvt_pk_bf16_f32 v12, v16, v17
	v_cvt_pk_bf16_f32 v13, v64, v65
	v_cvt_pk_bf16_f32 v15, v74, v75
	v_cvt_pk_bf16_f32 v10, v58, v59
	v_cvt_pk_bf16_f32 v4, v62, v63
	s_waitcnt lgkmcnt(2)
	v_mfma_f32_32x32x16_bf16 v[34:49], v[50:53], v[76:79], v[34:49]
	v_cvt_pk_bf16_f32 v5, v60, v61
	v_cvt_pk_bf16_f32 v6, v72, v73
	v_cvt_pk_bf16_f32 v7, v66, v67
	s_waitcnt lgkmcnt(0)
	v_mfma_f32_32x32x16_bf16 v[18:33], v[54:57], v[76:79], v[18:33]
	ds_read_b64_tr_b16 v[50:51], v70 offset:25600
	ds_read_b64_tr_b16 v[52:53], v70 offset:26112
	ds_read_b64_tr_b16 v[54:55], v70 offset:29696
	ds_read_b64_tr_b16 v[56:57], v70 offset:30208
	s_waitcnt lgkmcnt(2)
	v_mfma_f32_32x32x16_bf16 v[34:49], v[50:53], v[12:15], v[34:49]
	s_waitcnt lgkmcnt(0)
	v_mfma_f32_32x32x16_bf16 v[18:33], v[54:57], v[12:15], v[18:33]
	ds_read_b64_tr_b16 v[12:13], v70 offset:26624
	ds_read_b64_tr_b16 v[14:15], v70 offset:27136
	ds_read_b64_tr_b16 v[50:51], v70 offset:30720
	ds_read_b64_tr_b16 v[52:53], v70 offset:31232
	s_waitcnt lgkmcnt(2)
	v_mfma_f32_32x32x16_bf16 v[34:49], v[12:15], v[8:11], v[34:49]
	s_waitcnt lgkmcnt(0)
	v_mfma_f32_32x32x16_bf16 v[18:33], v[50:53], v[8:11], v[18:33]
	ds_read_b64_tr_b16 v[8:9], v70 offset:27648
	ds_read_b64_tr_b16 v[10:11], v70 offset:28160
	ds_read_b64_tr_b16 v[12:13], v70 offset:31744
	ds_read_b64_tr_b16 v[14:15], v70 offset:32256
	s_waitcnt lgkmcnt(2)
	v_mfma_f32_32x32x16_bf16 v[34:49], v[8:11], v[4:7], v[34:49]
	s_waitcnt lgkmcnt(0)
	v_mfma_f32_32x32x16_bf16 v[18:33], v[12:15], v[4:7], v[18:33]
	s_cbranch_scc1 .LBB0_640
	s_cmp_gt_u32 s78, 7
	s_cselect_b64 s[94:95], -1, 0
	s_cmp_gt_u32 s82, 3
	s_cselect_b64 s[96:97], -1, 0
	s_sub_i32 s0, 3, s80
	s_mov_b32 s1, s16
	s_lshl_b64 s[0:1], s[0:1], 13
	v_readlane_b32 s9, v251, 59
	s_add_u32 s2, s9, s0
	v_readlane_b32 s10, v251, 61
	s_addc_u32 s3, s10, s1
	s_add_i32 s0, s79, 4
	s_mov_b32 s1, s16
	s_lshl_b64 s[0:1], s[0:1], 13
	v_writelane_b32 v249, s40, 10
	s_add_u32 s7, s92, s0
	s_mov_b32 s12, s16
	s_addc_u32 s8, s93, s1
	s_mov_b32 s1, s16
	v_writelane_b32 v249, s12, 11
	s_cmp_gt_u32 s82, 4
	s_cselect_b64 s[4:5], -1, 0
	v_writelane_b32 v249, s13, 12
	s_sub_i32 s0, 4, s80
	v_writelane_b32 v249, s14, 13
	s_lshl_b64 s[0:1], s[0:1], 13
	v_writelane_b32 v249, s15, 14
	s_add_u32 s9, s9, s0
	v_writelane_b32 v249, s16, 15
	s_addc_u32 s10, s10, s1
	s_add_i32 s0, s79, 5
	v_writelane_b32 v249, s17, 16
	s_mov_b32 s1, s16
	v_writelane_b32 v249, s18, 17
	s_lshl_b64 s[0:1], s[0:1], 13
	v_writelane_b32 v249, s19, 18
	s_add_u32 s0, s92, s0
	v_writelane_b32 v249, s20, 19
	s_addc_u32 s1, s93, s1
	s_sub_i32 s11, 30, s6
	v_writelane_b32 v249, s21, 20
	s_cmp_gt_i32 s80, 3
	v_writelane_b32 v249, s22, 21
	s_cselect_b32 s2, s7, s2
	v_writelane_b32 v249, s23, 22
	s_cselect_b32 s3, s8, s3
	s_add_u32 s2, s2, s90
	v_writelane_b32 v249, s24, 23
	s_addc_u32 s3, s3, s91
	v_writelane_b32 v249, s25, 24
	s_cmp_gt_i32 s80, 4
	v_writelane_b32 v249, s26, 25
	s_cselect_b32 s0, s0, s9
	v_writelane_b32 v249, s27, 26
	s_cselect_b32 s1, s1, s10
	s_add_u32 s12, s0, s90
	s_addc_u32 s13, s1, s91
	v_cmp_eq_u32_e32 vcc, 0, v198
	v_cmp_eq_u32_e64 s[0:1], s78, v198
	s_or_b64 s[0:1], vcc, s[0:1]
	v_cmp_eq_u32_e32 vcc, s11, v198
	s_or_b64 s[8:9], s[0:1], vcc
	v_readlane_b32 s0, v250, 44
	v_and_b32_e32 v4, 0x3fffffe0, v68
	v_lshl_add_u64 v[186:187], s[2:3], 0, v[184:185]
	v_lshl_add_u32 v206, v68, 2, s0
	v_lshl_add_u32 v207, v4, 2, s0
	s_mov_b64 s[0:1], 0x800000
	v_lshl_add_u64 v[190:191], s[12:13], 0, v[184:185]
	v_sub_u32_e32 v208, v71, v69
	v_lshl_add_u64 v[188:189], v[186:187], 0, s[0:1]
	v_lshl_add_u64 v[192:193], v[190:191], 0, s[0:1]
	v_mul_lo_u32 v3, v3, s64
	v_lshlrev_b32_e32 v4, 2, v198
	v_readlane_b32 s0, v250, 47
	v_lshlrev_b32_e32 v50, 2, v71
	v_mov_b32_e32 v16, v2
	v_add3_u32 v209, s0, v3, v4
	v_cmp_gt_i32_e64 s[0:1], 1, v208
	v_mov_b32_e32 v17, v2
	s_sub_i32 s83, s80, s6
	v_writelane_b32 v249, s0, 27
	v_mov_b32_e32 v3, v2
	v_mov_b32_e32 v4, v2
	v_writelane_b32 v249, s1, 28
	v_cmp_gt_i32_e64 s[0:1], 0, v208
	v_mov_b32_e32 v5, v2
	v_mov_b32_e32 v6, v2
	v_writelane_b32 v249, s0, 29
	v_mov_b32_e32 v7, v2
	v_mov_b32_e32 v8, v2
	v_writelane_b32 v249, s1, 30
	v_cmp_gt_i32_e64 s[0:1], 33, v208
	v_mov_b32_e32 v9, v2
	v_mov_b32_e32 v10, v2
	v_writelane_b32 v249, s0, 31
	v_mov_b32_e32 v11, v2
	v_mov_b32_e32 v12, v2
	v_writelane_b32 v249, s1, 32
	v_cmp_gt_i32_e64 s[0:1], 32, v208
	v_mov_b32_e32 v13, v2
	v_mov_b32_e32 v14, v2
	v_writelane_b32 v249, s0, 33
	v_mov_b32_e32 v15, v2
	v_add_u32_e32 v50, 0, v50
	v_writelane_b32 v249, s1, 34
	v_cmp_gt_i32_e64 s[0:1], 3, v208
	v_mov_b64_e32 v[96:97], v[16:17]
	v_mov_b64_e32 v[112:113], v[16:17]
	v_writelane_b32 v249, s0, 35
	s_add_i32 s83, s83, 32
	v_cmp_lt_u32_e64 s[6:7], s78, v198
	v_writelane_b32 v249, s1, 36
	v_cmp_gt_i32_e64 s[0:1], 2, v208
	v_mov_b32_e32 v211, 0
	v_cmp_eq_u32_e64 s[10:11], 0, v68
	v_writelane_b32 v249, s0, 37
	v_cmp_ne_u32_e64 s[12:13], 0, v198
	v_cmp_lt_u32_e64 s[14:15], 1, v198
	v_writelane_b32 v249, s1, 38
	v_cmp_gt_i32_e64 s[0:1], 35, v208
	v_cmp_lt_u32_e64 s[16:17], 2, v198
	v_cmp_lt_u32_e64 s[18:19], 3, v198
	v_writelane_b32 v249, s0, 39
	v_cmp_lt_u32_e64 s[20:21], 4, v198
	v_cmp_lt_u32_e64 s[22:23], 5, v198
	v_writelane_b32 v249, s1, 40
	v_cmp_gt_i32_e64 s[0:1], 34, v208
	v_cmp_lt_u32_e64 s[24:25], 6, v198
	v_cmp_lt_u32_e64 s[26:27], 7, v198
	v_writelane_b32 v249, s0, 41
	v_cmp_lt_u32_e64 s[28:29], 8, v198
	v_cmp_lt_u32_e64 s[30:31], 9, v198
	v_writelane_b32 v249, s1, 42
	v_cmp_gt_i32_e64 s[0:1], 9, v208
	v_cmp_lt_u32_e64 s[34:35], 10, v198
	v_cmp_lt_u32_e64 s[36:37], 11, v198
	v_writelane_b32 v249, s0, 43
	v_cmp_lt_u32_e64 s[38:39], 12, v198
	v_cmp_lt_u32_e64 s[40:41], 13, v198
	v_writelane_b32 v249, s1, 44
	v_cmp_gt_i32_e64 s[0:1], 8, v208
	v_cmp_lt_u32_e64 s[42:43], 14, v198
	v_cmp_lt_u32_e64 s[44:45], 15, v198
	v_writelane_b32 v249, s0, 45
	v_cmp_lt_u32_e64 s[46:47], 16, v198
	v_cmp_lt_u32_e64 s[48:49], 17, v198
	v_writelane_b32 v249, s1, 46
	v_cmp_gt_i32_e64 s[0:1], 41, v208
	v_cmp_lt_u32_e64 s[50:51], 18, v198
	v_cmp_lt_u32_e64 s[52:53], 19, v198
	v_writelane_b32 v249, s0, 47
	v_cmp_lt_u32_e64 s[54:55], 20, v198
	v_cmp_lt_u32_e64 s[56:57], 21, v198
	v_writelane_b32 v249, s1, 48
	v_cmp_gt_i32_e64 s[0:1], 40, v208
	v_cmp_lt_u32_e64 s[58:59], 22, v198
	v_cmp_lt_u32_e64 s[60:61], 23, v198
	v_writelane_b32 v249, s0, 49
	v_cmp_lt_u32_e64 s[62:63], 24, v198
	s_mov_b32 s2, 0
	v_writelane_b32 v249, s1, 50
	v_cmp_gt_i32_e64 s[0:1], 11, v208
	v_mov_b32_e32 v214, 0
	v_add_u32_e32 v210, 0x20400, v50
	v_writelane_b32 v249, s0, 51
	v_mov_b32_e32 v114, 0
	v_mov_b64_e32 v[94:95], v[14:15]
	v_writelane_b32 v249, s1, 52
	v_cmp_gt_i32_e64 s[0:1], 10, v208
	v_mov_b64_e32 v[92:93], v[12:13]
	v_mov_b64_e32 v[90:91], v[10:11]
	v_writelane_b32 v249, s0, 53
	v_mov_b64_e32 v[88:89], v[8:9]
	v_mov_b64_e32 v[86:87], v[6:7]
	v_writelane_b32 v249, s1, 54
	v_cmp_gt_i32_e64 s[0:1], 43, v208
	v_mov_b64_e32 v[84:85], v[4:5]
	v_mov_b64_e32 v[82:83], v[2:3]
	v_writelane_b32 v249, s0, 55
	v_mov_b64_e32 v[110:111], v[14:15]
	v_mov_b64_e32 v[108:109], v[12:13]
	v_writelane_b32 v249, s1, 56
	v_cmp_gt_i32_e64 s[0:1], 42, v208
	v_mov_b64_e32 v[106:107], v[10:11]
	v_mov_b64_e32 v[104:105], v[8:9]
	v_writelane_b32 v249, s0, 57
	v_mov_b64_e32 v[102:103], v[6:7]
	v_mov_b64_e32 v[100:101], v[4:5]
	v_writelane_b32 v249, s1, 58
	v_cmp_gt_i32_e64 s[0:1], 17, v208
	v_mov_b64_e32 v[98:99], v[2:3]
	v_cmp_lt_u32_e64 s[64:65], 25, v198
	v_writelane_b32 v249, s0, 59
	v_cmp_lt_u32_e64 s[66:67], 26, v198
	v_cmp_lt_u32_e64 s[68:69], 27, v198
	v_writelane_b32 v249, s1, 60
	v_cmp_gt_i32_e64 s[0:1], 16, v208
	v_cmp_lt_u32_e64 s[70:71], 28, v198
	v_cmp_lt_u32_e64 s[72:73], 29, v198
	v_writelane_b32 v249, s0, 61
	v_cmp_eq_u32_e64 s[74:75], 31, v198
	s_nop 0
	v_writelane_b32 v249, s1, 62
	v_cmp_gt_i32_e64 s[0:1], 49, v208
	s_nop 1
	v_writelane_b32 v249, s0, 63
	s_nop 1
	v_writelane_b32 v248, s1, 0
	v_cmp_gt_i32_e64 s[0:1], 48, v208
	s_nop 1
	v_writelane_b32 v248, s0, 1
	s_nop 1
	v_writelane_b32 v248, s1, 2
	v_cmp_gt_i32_e64 s[0:1], 19, v208
	s_nop 1
	v_writelane_b32 v248, s0, 3
	s_nop 1
	v_writelane_b32 v248, s1, 4
	v_cmp_gt_i32_e64 s[0:1], 18, v208
	s_nop 1
	v_writelane_b32 v248, s0, 5
	s_nop 1
	v_writelane_b32 v248, s1, 6
	v_cmp_gt_i32_e64 s[0:1], 51, v208
	s_nop 1
	v_writelane_b32 v248, s0, 7
	s_nop 1
	v_writelane_b32 v248, s1, 8
	v_cmp_gt_i32_e64 s[0:1], 50, v208
	s_nop 1
	v_writelane_b32 v248, s0, 9
	s_nop 1
	v_writelane_b32 v248, s1, 10
	v_cmp_gt_i32_e64 s[0:1], 25, v208
	s_nop 1
	v_writelane_b32 v248, s0, 11
	s_nop 1
	v_writelane_b32 v248, s1, 12
	v_cmp_gt_i32_e64 s[0:1], 24, v208
	s_nop 1
	v_writelane_b32 v248, s0, 13
	s_nop 1
	v_writelane_b32 v248, s1, 14
	v_cmp_gt_i32_e64 s[0:1], 57, v208
	s_nop 1
	v_writelane_b32 v248, s0, 15
	s_nop 1
	v_writelane_b32 v248, s1, 16
	v_cmp_gt_i32_e64 s[0:1], 56, v208
	s_nop 1
	v_writelane_b32 v248, s0, 17
	s_nop 1
	v_writelane_b32 v248, s1, 18
	v_cmp_gt_i32_e64 s[0:1], 27, v208
	s_nop 1
	v_writelane_b32 v248, s0, 19
	s_nop 1
	v_writelane_b32 v248, s1, 20
	v_cmp_gt_i32_e64 s[0:1], 26, v208
	s_nop 1
	v_writelane_b32 v248, s0, 21
	s_nop 1
	v_writelane_b32 v248, s1, 22
	v_cmp_gt_i32_e64 s[0:1], 59, v208
	s_nop 1
	v_writelane_b32 v248, s0, 23
	s_nop 1
	v_writelane_b32 v248, s1, 24
	v_cmp_gt_i32_e64 s[0:1], 58, v208
	s_nop 1
	v_writelane_b32 v248, s0, 25
	s_nop 1
	v_writelane_b32 v248, s1, 26
	v_mov_b64_e32 v[50:51], 0
	v_mov_b64_e32 v[52:53], 0
	v_mov_b64_e32 v[54:55], 0
	v_mov_b64_e32 v[56:57], 0
	v_mov_b64_e32 v[58:59], 0
	v_mov_b64_e32 v[60:61], 0
	v_mov_b64_e32 v[62:63], 0
	v_mov_b64_e32 v[64:65], 0
	v_mov_b64_e32 v[66:67], 0
	v_mov_b64_e32 v[68:69], 0
	v_mov_b64_e32 v[70:71], 0
	v_mov_b64_e32 v[72:73], 0
	v_mov_b64_e32 v[74:75], 0
	v_mov_b64_e32 v[76:77], 0
	v_mov_b64_e32 v[78:79], 0
	v_mov_b64_e32 v[80:81], 0
	s_mov_b32 s32, 0x8000
	s_add_i32 s99, s82, -5
	s_max_i32 s99, s99, 0
	s_cmp_gt_i32 s80, 5
	s_cbranch_scc1 .Lnsa_e6_win
	s_sub_i32 s0, 5, s80
	s_lshl_b32 s0, s0, 13
	v_readlane_b32 s100, v251, 59
	v_readlane_b32 s101, v251, 61
	s_branch .Lnsa_e6_done
.Lnsa_e6_win:
	s_add_i32 s0, s79, 6
	s_lshl_b32 s0, s0, 13
	s_mov_b32 s100, s92
	s_mov_b32 s101, s93
.Lnsa_e6_done:
	s_add_u32 s100, s100, s0
	s_addc_u32 s101, s101, 0
	s_add_u32 s100, s100, s90
	s_addc_u32 s101, s101, s91
.LBB0_574:
	s_add_i32 s0, s2, -1
	s_cmp_lt_u32 s0, s99
	s_cbranch_scc0 .Lnsa_step_general
	s_waitcnt vmcnt(8) lgkmcnt(0)
	s_barrier
	s_mov_b64 s[86:87], 0
	v_lshl_add_u64 v[4:5], s[100:101], 0, v[184:185]
	s_add_i32 s3, s32, 0x14000
	s_cmp_ge_u32 s3, 0x18000
	s_cselect_b32 s1, 0x18000, 0
	s_sub_i32 s3, s3, s1
	v_readlane_b32 s76, v251, 57
	s_mov_b64 s[0:1], 0x800000
	s_add_i32 m0, s76, s3
	s_add_u32 s100, s100, 0x2000
	s_addc_u32 s101, s101, 0
	global_load_lds_dwordx4 v[4:5], off
	v_lshl_add_u64 v[4:5], v[4:5], 0, s[0:1]
	s_add_i32 m0, m0, 0x2000
	s_add_i32 s0, s2, 5
	s_cmp_lg_u32 s0, s80
	global_load_lds_dwordx4 v[4:5], off
	s_cbranch_scc1 .LBB0_599
	v_readlane_b32 s100, v251, 59
	v_readlane_b32 s101, v251, 61
	s_add_u32 s100, s100, s90
	s_addc_u32 s101, s101, s91
	s_branch .LBB0_599

.LBB0_602:
	s_mov_b32 s3, s32
	s_cmp_gt_u32 s2, s80
	s_mov_b64 s[0:1], -1
	s_cbranch_scc1 .LBB0_617
	s_add_i32 s76, s2, s79
	s_cmp_eq_u32 s78, s76
	s_cselect_b64 s[0:1], -1, 0
	s_and_b64 vcc, s[94:95], s[86:87]
	s_or_b64 vcc, s[0:1], vcc
	s_mov_b64 s[0:1], -1
	s_and_b64 vcc, exec, vcc
	s_cbranch_vccnz .LBB0_607
	v_add3_u32 v16, s3, v203, v202
	ds_read_b128 v[4:7], v16
	ds_read_b128 v[8:11], v16 offset:512
	ds_read_b128 v[12:15], v16 offset:2048
	ds_read_b128 v[82:85], v16 offset:2560
	ds_read_b128 v[86:89], v16 offset:4096
	ds_read_b128 v[90:93], v16 offset:4608
	ds_read_b128 v[94:97], v16 offset:6144
	ds_read_b128 v[98:101], v16 offset:6656
	v_xor_b32_e32 v114, 0x80000000, v3
	v_mov_b32_e32 v115, v114
	v_mov_b32_e32 v116, v114
	v_mov_b32_e32 v117, v114
	v_mov_b32_e32 v118, v114
	v_mov_b32_e32 v119, v114
	v_mov_b32_e32 v120, v114
	v_mov_b32_e32 v121, v114
	v_mov_b32_e32 v122, v114
	v_mov_b32_e32 v123, v114
	v_mov_b32_e32 v124, v114
	v_mov_b32_e32 v125, v114
	v_mov_b32_e32 v126, v114
	v_mov_b32_e32 v127, v114
	v_mov_b32_e32 v128, v114
	v_mov_b32_e32 v129, v114
	s_waitcnt lgkmcnt(7)
	s_nop 0
	v_mfma_f32_32x32x16_bf16 v[130:145], v[4:7], v[158:161], v[114:129]
	v_add_u32_e32 v4, s3, v204
	v_add3_u32 v6, v4, v201, v205
	s_waitcnt lgkmcnt(6)
	v_mfma_f32_32x32x16_bf16 v[114:129], v[8:11], v[158:161], v[114:129]
	s_waitcnt lgkmcnt(5)
	v_mfma_f32_32x32x16_bf16 v[130:145], v[12:15], v[154:157], v[130:145]
	ds_read_b64_tr_b16 v[178:179], v6 offset:8192
	ds_read_b64_tr_b16 v[180:181], v6 offset:8704
	ds_read_b64_tr_b16 v[174:175], v6 offset:12288
	ds_read_b64_tr_b16 v[176:177], v6 offset:12800
	ds_read_b64_tr_b16 v[170:171], v6 offset:9216
	ds_read_b64_tr_b16 v[172:173], v6 offset:9728
	ds_read_b64_tr_b16 v[166:167], v6 offset:13312
	ds_read_b64_tr_b16 v[168:169], v6 offset:13824
	ds_read_b64_tr_b16 v[162:163], v6 offset:10240
	ds_read_b64_tr_b16 v[164:165], v6 offset:10752
	ds_read_b64_tr_b16 v[12:13], v6 offset:14336
	ds_read_b64_tr_b16 v[14:15], v6 offset:14848
	ds_read_b64_tr_b16 v[8:9], v6 offset:11264
	ds_read_b64_tr_b16 v[10:11], v6 offset:11776
	ds_read_b64_tr_b16 v[4:5], v6 offset:15360
	ds_read_b64_tr_b16 v[6:7], v6 offset:15872
	s_waitcnt lgkmcnt(14)
	v_mfma_f32_32x32x16_bf16 v[114:129], v[82:85], v[154:157], v[114:129]
	v_mfma_f32_32x32x16_bf16 v[130:145], v[86:89], v[150:153], v[130:145]
	v_mfma_f32_32x32x16_bf16 v[114:129], v[90:93], v[150:153], v[114:129]
	v_mfma_f32_32x32x16_bf16 v[130:145], v[94:97], v[146:149], v[130:145]
	v_mfma_f32_32x32x16_bf16 v[114:129], v[98:101], v[146:149], v[114:129]
	s_nop 10
	v_max_f32_e32 v16, v131, v131
	v_max_f32_e32 v17, v130, v130
	v_max_f32_e32 v16, v17, v16
	v_max3_f32 v17, v132, v133, v115
	v_max3_f32 v16, v16, v114, v116
	v_max3_f32 v16, v16, v117, v134
	v_max3_f32 v17, v17, v136, v137
	v_max3_f32 v16, v16, v135, v118
	v_max3_f32 v17, v17, v120, v121
	v_max3_f32 v16, v16, v119, v138
	v_max3_f32 v17, v17, v140, v141
	v_max3_f32 v16, v16, v139, v122
	v_max3_f32 v17, v17, v124, v125
	v_max3_f32 v16, v16, v123, v142
	v_max3_f32 v17, v17, v144, v145
	v_max3_f32 v16, v16, v143, v126
	v_max3_f32 v17, v17, v128, v129
	v_max3_f32 v16, v16, v127, v17
	v_mov_b32_e32 v17, v16
	s_nop 1
	v_permlane32_swap_b32_e32 v16, v17
	v_max_f32_e32 v17, v17, v17
	v_max_f32_e32 v16, v16, v16
	v_max_f32_e32 v17, v16, v17
	s_mov_b32 s0, 0x41000000
	v_cmp_lt_f32_e32 vcc, s0, v17
	s_cmp_lg_u64 vcc, 0
	s_cselect_b64 s[0:1], -1, 0
	s_or_b64 s[0:1], s[86:87], s[0:1]
	s_and_b64 vcc, exec, s[0:1]
	v_mov_b32_e32 v16, v213
	v_mov_b32_e32 v214, v3
	s_cbranch_vccz .LBB0_606
	v_cndmask_b32_e64 v16, 0, v197, s[86:87]
	v_max_f32_e32 v17, v17, v17
	v_max_f32_e32 v16, v17, v16
	v_exp_f32_e64 v216, -v16
	v_add_f32_e32 v214, v3, v16
	v_pk_add_f32 v[130:131], v[130:131], v[16:17] op_sel_hi:[1,0] neg_lo:[0,1] neg_hi:[0,1]
	v_pk_add_f32 v[114:115], v[114:115], v[16:17] op_sel_hi:[1,0] neg_lo:[0,1] neg_hi:[0,1]
	v_pk_add_f32 v[132:133], v[132:133], v[16:17] op_sel_hi:[1,0] neg_lo:[0,1] neg_hi:[0,1]
	v_pk_add_f32 v[116:117], v[116:117], v[16:17] op_sel_hi:[1,0] neg_lo:[0,1] neg_hi:[0,1]
	v_pk_add_f32 v[134:135], v[134:135], v[16:17] op_sel_hi:[1,0] neg_lo:[0,1] neg_hi:[0,1]
	v_pk_add_f32 v[118:119], v[118:119], v[16:17] op_sel_hi:[1,0] neg_lo:[0,1] neg_hi:[0,1]
	v_pk_add_f32 v[136:137], v[136:137], v[16:17] op_sel_hi:[1,0] neg_lo:[0,1] neg_hi:[0,1]
	v_pk_add_f32 v[120:121], v[120:121], v[16:17] op_sel_hi:[1,0] neg_lo:[0,1] neg_hi:[0,1]
	v_pk_add_f32 v[138:139], v[138:139], v[16:17] op_sel_hi:[1,0] neg_lo:[0,1] neg_hi:[0,1]
	v_pk_add_f32 v[122:123], v[122:123], v[16:17] op_sel_hi:[1,0] neg_lo:[0,1] neg_hi:[0,1]
	v_pk_add_f32 v[140:141], v[140:141], v[16:17] op_sel_hi:[1,0] neg_lo:[0,1] neg_hi:[0,1]
	v_pk_add_f32 v[124:125], v[124:125], v[16:17] op_sel_hi:[1,0] neg_lo:[0,1] neg_hi:[0,1]
	v_pk_add_f32 v[142:143], v[142:143], v[16:17] op_sel_hi:[1,0] neg_lo:[0,1] neg_hi:[0,1]
	v_pk_add_f32 v[126:127], v[126:127], v[16:17] op_sel_hi:[1,0] neg_lo:[0,1] neg_hi:[0,1]
	v_pk_add_f32 v[144:145], v[144:145], v[16:17] op_sel_hi:[1,0] neg_lo:[0,1] neg_hi:[0,1]
	v_pk_add_f32 v[128:129], v[128:129], v[16:17] op_sel_hi:[1,0] neg_lo:[0,1] neg_hi:[0,1]
	v_pk_mul_f32 v[80:81], v[80:81], v[216:217] op_sel_hi:[1,0]
	v_pk_mul_f32 v[78:79], v[78:79], v[216:217] op_sel_hi:[1,0]
	v_pk_mul_f32 v[76:77], v[76:77], v[216:217] op_sel_hi:[1,0]
	v_pk_mul_f32 v[74:75], v[74:75], v[216:217] op_sel_hi:[1,0]
	v_pk_mul_f32 v[72:73], v[72:73], v[216:217] op_sel_hi:[1,0]
	v_pk_mul_f32 v[70:71], v[70:71], v[216:217] op_sel_hi:[1,0]
	v_pk_mul_f32 v[68:69], v[68:69], v[216:217] op_sel_hi:[1,0]
	v_pk_mul_f32 v[66:67], v[66:67], v[216:217] op_sel_hi:[1,0]
	v_pk_mul_f32 v[64:65], v[64:65], v[216:217] op_sel_hi:[1,0]
	v_pk_mul_f32 v[62:63], v[62:63], v[216:217] op_sel_hi:[1,0]
	v_pk_mul_f32 v[60:61], v[60:61], v[216:217] op_sel_hi:[1,0]
	v_pk_mul_f32 v[58:59], v[58:59], v[216:217] op_sel_hi:[1,0]
	v_pk_mul_f32 v[56:57], v[56:57], v[216:217] op_sel_hi:[1,0]
	v_pk_mul_f32 v[54:55], v[54:55], v[216:217] op_sel_hi:[1,0]
	v_pk_mul_f32 v[52:53], v[52:53], v[216:217] op_sel_hi:[1,0]
	v_pk_mul_f32 v[50:51], v[50:51], v[216:217] op_sel_hi:[1,0]
	v_mul_f32_e32 v16, v213, v216

.LBB0_626:
	s_add_i32 s0, s2, 1
	s_cmp_eq_u32 s2, s83
	s_cbranch_scc1 .LBB0_558
	s_add_i32 s32, s32, 0x4000
	s_cmp_eq_u32 s32, 0x18000
	s_cselect_b32 s32, 0, s32
	s_mov_b32 s2, s0
	s_branch .LBB0_574

	.amdhsa_kernel _Z10hybrid_fwd4Args
		.amdhsa_group_segment_fixed_size 0
		.amdhsa_private_segment_fixed_size 0
		.amdhsa_kernarg_size 448
		.amdhsa_user_sgpr_count 2
		.amdhsa_user_sgpr_dispatch_ptr 0
		.amdhsa_user_sgpr_queue_ptr 0
		.amdhsa_user_sgpr_kernarg_segment_ptr 1
		.amdhsa_user_sgpr_dispatch_id 0
		.amdhsa_user_sgpr_kernarg_preload_length 0
		.amdhsa_user_sgpr_kernarg_preload_offset 0
		.amdhsa_user_sgpr_private_segment_size 0
		.amdhsa_uses_dynamic_stack 0
		.amdhsa_enable_private_segment 0
		.amdhsa_system_sgpr_workgroup_id_x 1
		.amdhsa_system_sgpr_workgroup_id_y 0
		.amdhsa_system_sgpr_workgroup_id_z 0
		.amdhsa_system_sgpr_workgroup_info 0
		.amdhsa_system_vgpr_workitem_id 0
		.amdhsa_next_free_vgpr 252
		.amdhsa_next_free_sgpr 102
		.amdhsa_accum_offset 252
		.amdhsa_reserve_vcc 1
		.amdhsa_float_round_mode_32 0
		.amdhsa_float_round_mode_16_64 0
		.amdhsa_float_denorm_mode_32 3
		.amdhsa_float_denorm_mode_16_64 3
		.amdhsa_dx10_clamp 1
		.amdhsa_ieee_mode 1
		.amdhsa_fp16_overflow 0
		.amdhsa_tg_split 0
		.amdhsa_exception_fp_ieee_invalid_op 0
		.amdhsa_exception_fp_denorm_src 0
		.amdhsa_exception_fp_ieee_div_zero 0
		.amdhsa_exception_fp_ieee_overflow 0
		.amdhsa_exception_fp_ieee_underflow 0
		.amdhsa_exception_fp_ieee_inexact 0
		.amdhsa_exception_int_div_zero 0
	.end_amdhsa_kernel

amdhsa.kernels:
  - .agpr_count:     0
    .args:
      - .offset:         0
        .size:           192
        .value_kind:     by_value
      - .offset:         192
        .size:           4
        .value_kind:     hidden_block_count_x
      - .offset:         196
        .size:           4
        .value_kind:     hidden_block_count_y
      - .offset:         200
        .size:           4
        .value_kind:     hidden_block_count_z
      - .offset:         204
        .size:           2
        .value_kind:     hidden_group_size_x
      - .offset:         206
        .size:           2
        .value_kind:     hidden_group_size_y
      - .offset:         208
        .size:           2
        .value_kind:     hidden_group_size_z
      - .offset:         210
        .size:           2
        .value_kind:     hidden_remainder_x
      - .offset:         212
        .size:           2
        .value_kind:     hidden_remainder_y
      - .offset:         214
        .size:           2
        .value_kind:     hidden_remainder_z
      - .offset:         232
        .size:           8
        .value_kind:     hidden_global_offset_x
      - .offset:         240
        .size:           8
        .value_kind:     hidden_global_offset_y
      - .offset:         248
        .size:           8
        .value_kind:     hidden_global_offset_z
      - .offset:         256
        .size:           2
        .value_kind:     hidden_grid_dims
      - .offset:         312
        .size:           4
        .value_kind:     hidden_dynamic_lds_size
    .group_segment_fixed_size: 0
    .kernarg_segment_align: 8
    .kernarg_segment_size: 448
    .language:       OpenCL C
    .language_version:
      - 2
      - 0
    .max_flat_workgroup_size: 512
    .name:           _Z10hybrid_fwd4Args
    .private_segment_fixed_size: 0
    .sgpr_count:     108
    .sgpr_spill_count: 299
    .symbol:         _Z10hybrid_fwd4Args.kd
    .uniform_work_group_size: 1
    .uses_dynamic_stack: false
    .vgpr_count:     252
    .vgpr_spill_count: 0
    .wavefront_size: 64
